# proj phase: half of each XCD's workgroups start about half a tile later so that the epilogue store bursts of the two groups do not coincide
# baseline (speedup 1.0000x reference)
.LBB0_225:
	s_andn2_b64 vcc, exec, s[0:1]
	v_writelane_b32 v252, s46, 58
	s_cbranch_vccnz .LBB0_390
	v_readlane_b32 s100, v251, 0
	s_nop 3
	s_bitcmp1_b32 s100, 3
	s_cbranch_scc0 .Lnostag1
	s_sleep 127
	s_sleep 127
	s_sleep 40
.Lnostag1:
	v_readlane_b32 s4, v251, 4
	v_readlane_b32 s0, v251, 49
	v_readlane_b32 s5, v251, 5
	v_mov_b32_e32 v1, v0
	s_waitcnt vmcnt(0)
	v_mov_b32_e32 v12, v0
	v_readlane_b32 s1, v251, 50
	s_andn2_b64 vcc, exec, s[0:1]
	v_readfirstlane_b32 s17, v12
	s_cbranch_vccnz .LBB0_344
	v_lshlrev_b32_e32 v1, 4, v12
	v_add_u32_e32 v3, 0x2000, v1
	v_ashrrev_i32_e32 v4, 31, v3
	v_lshrrev_b32_e32 v4, 22, v4
	v_add_u32_e32 v4, v3, v4
	v_ashrrev_i32_e32 v13, 10, v4
	v_mul_i32_i24_e32 v4, 0x400, v13
	s_load_dwordx2 s[12:13], s[4:5], 0xc8
	s_load_dwordx4 s[0:3], s[4:5], 0x40
	v_sub_u32_e32 v3, v3, v4
	v_lshrrev_b32_e32 v4, 4, v3
	v_bitop3_b32 v3, v4, v3, 32 bitop3:0x6c
	v_ashrrev_i32_e32 v4, 31, v3
	s_waitcnt lgkmcnt(0)
	s_add_u32 s30, s12, 0xd400000
	v_lshrrev_b32_e32 v4, 26, v4
	s_mul_i32 s4, s46, 0x500000
	s_addc_u32 s31, s13, 0
	v_add_u32_e32 v4, v3, v4
	v_lshlrev_b32_e32 v5, 3, v13
	s_add_u32 s4, s12, s4
	v_ashrrev_i32_e32 v14, 6, v4
	v_and_b32_e32 v5, -16, v5
	s_addc_u32 s5, s13, 0
	v_add_u32_e32 v5, v14, v5
	s_add_u32 s34, s4, 0x1c00000
	v_and_b32_e32 v6, 3, v14
	s_mov_b32 s4, 0x3fffe0
	v_lshrrev_b32_e32 v7, 2, v5
	v_lshlrev_b32_e32 v8, 1, v5
	v_and_b32_e32 v4, 0xc0, v4
	v_and_or_b32 v6, v5, s4, v6
	v_and_b32_e32 v7, 4, v7
	v_and_b32_e32 v8, 24, v8
	v_sub_u32_e32 v3, v3, v4
	v_or3_b32 v6, v6, v7, v8
	v_lshlrev_b32_e32 v7, 5, v13
	v_ashrrev_i16_sdwa v3, v211, sext(v3) dst_sel:DWORD dst_unused:UNUSED_PAD src0_sel:DWORD src1_sel:BYTE_0
	v_and_b32_e32 v7, 32, v7
	v_bfe_i32 v15, v3, 0, 16
	v_add_lshl_u32 v3, v7, v15, 1
	v_lshl_add_u32 v172, v6, 10, v3
	v_lshl_add_u32 v174, v5, 10, v3
	v_bfe_i32 v3, v12, 27, 1
	v_lshrrev_b32_e32 v3, 22, v3
	v_add_u32_e32 v3, v1, v3
	v_and_b32_e32 v3, 0xfffffc00, v3
	v_sub_u32_e32 v1, v1, v3
	v_lshrrev_b32_e32 v3, 4, v1
	v_ashrrev_i32_e32 v4, 31, v12
	v_bitop3_b32 v1, v3, v1, 32 bitop3:0x6c
	v_lshrrev_b32_e32 v4, 26, v4
	v_ashrrev_i32_e32 v3, 31, v1
	v_add_u32_e32 v4, v12, v4
	v_lshrrev_b32_e32 v3, 26, v3
	v_ashrrev_i32_e32 v17, 6, v4
	v_add_u32_e32 v3, v1, v3
	v_lshlrev_b32_e32 v4, 3, v17
	v_ashrrev_i32_e32 v16, 6, v3
	v_and_b32_e32 v4, -16, v4
	s_addc_u32 s35, s5, 0
	s_ashr_i32 s18, s17, 6
	v_add_u32_e32 v4, v16, v4
	v_and_b32_e32 v5, 3, v16
	s_ashr_i32 s16, s17, 8
	s_lshl_b32 s36, s18, 10
	v_and_or_b32 v5, v4, s4, v5
	v_lshrrev_b32_e32 v6, 2, v4
	v_lshlrev_b32_e32 v7, 1, v4
	v_and_b32_e32 v3, 0xc0, v3
	v_readlane_b32 s4, v252, 46
	v_and_b32_e32 v6, 4, v6
	v_and_b32_e32 v7, 24, v7
	v_sub_u32_e32 v1, v1, v3
	v_readlane_b32 s5, v252, 47
	s_add_u32 s6, s30, s4
	v_or3_b32 v5, v5, v6, v7
	v_lshlrev_b32_e32 v6, 5, v17
	v_ashrrev_i16_sdwa v1, v211, sext(v1) dst_sel:DWORD dst_unused:UNUSED_PAD src0_sel:DWORD src1_sel:BYTE_0
	s_addc_u32 s7, s31, s5
	v_readlane_b32 s4, v252, 50
	v_and_b32_e32 v6, 32, v6
	v_bfe_i32 v18, v1, 0, 16
	v_readlane_b32 s5, v252, 51
	s_add_u32 s4, s34, s4
	v_add_lshl_u32 v1, v6, v18, 1
	s_addc_u32 s5, s35, s5
	s_add_i32 s37, s36, 0
	v_lshl_add_u32 v176, v5, 10, v1
	v_lshl_add_u32 v178, v4, 10, v1
	v_mov_b32_e32 v1, 0x7f7f7f7f
	s_add_i32 m0, s37, 0x10000
	v_mov_b32_e32 v177, v2
	global_load_lds_dwordx4 v176, s[4:5]
	s_add_i32 m0, s37, 0x12000
	s_add_u32 s8, s4, 0x20000
	global_load_lds_dwordx4 v172, s[4:5]
	s_addc_u32 s9, s5, 0
	s_add_i32 m0, s37, 0x14000
	s_add_i32 s38, s37, 0x2000
	global_load_lds_dwordx4 v176, s[8:9]
	s_add_i32 m0, s37, 0x16000
	v_mov_b32_e32 v173, v2
	global_load_lds_dwordx4 v172, s[8:9]
	s_mov_b32 m0, s37
	s_add_u32 s8, s6, 0x20000
	global_load_lds_dwordx4 v178, s[6:7]
	s_mov_b32 m0, s38
	s_addc_u32 s9, s7, 0
	s_add_i32 s39, s37, 0x4000
	global_load_lds_dwordx4 v174, s[6:7]
	s_mov_b32 m0, s39
	s_add_i32 s42, s37, 0x6000
	global_load_lds_dwordx4 v178, s[8:9]
	s_mov_b32 m0, s42
	v_mov_b32_e32 v179, v2
	global_load_lds_dwordx4 v174, s[8:9]
	v_mov_b32_e32 v175, v2
	s_cmp_eq_u32 s16, 1
	v_lshl_add_u64 v[10:11], s[4:5], 0, v[176:177]
	v_lshl_add_u64 v[8:9], s[4:5], 0, v[172:173]
	v_lshl_add_u64 v[4:5], s[6:7], 0, v[178:179]
	s_cselect_b64 s[8:9], -1, 0
	s_cmp_lg_u32 s16, 1
	v_lshl_add_u64 v[6:7], s[6:7], 0, v[174:175]
	s_cbranch_scc1 .LBB0_229
	s_barrier

	.amdhsa_kernel _Z3fwd4Args
		.amdhsa_group_segment_fixed_size 0
		.amdhsa_private_segment_fixed_size 0
		.amdhsa_kernarg_size 472
		.amdhsa_user_sgpr_count 2
		.amdhsa_user_sgpr_dispatch_ptr 0
		.amdhsa_user_sgpr_queue_ptr 0
		.amdhsa_user_sgpr_kernarg_segment_ptr 1
		.amdhsa_user_sgpr_dispatch_id 0
		.amdhsa_user_sgpr_kernarg_preload_length 0
		.amdhsa_user_sgpr_kernarg_preload_offset 0
		.amdhsa_user_sgpr_private_segment_size 0
		.amdhsa_uses_dynamic_stack 0
		.amdhsa_enable_private_segment 0
		.amdhsa_system_sgpr_workgroup_id_x 1
		.amdhsa_system_sgpr_workgroup_id_y 0
		.amdhsa_system_sgpr_workgroup_id_z 0
		.amdhsa_system_sgpr_workgroup_info 0
		.amdhsa_system_vgpr_workitem_id 0
		.amdhsa_next_free_vgpr 256
		.amdhsa_next_free_sgpr 102
		.amdhsa_accum_offset 256
		.amdhsa_reserve_vcc 1
		.amdhsa_float_round_mode_32 0
		.amdhsa_float_round_mode_16_64 0
		.amdhsa_float_denorm_mode_32 3
		.amdhsa_float_denorm_mode_16_64 3
		.amdhsa_dx10_clamp 1
		.amdhsa_ieee_mode 1
		.amdhsa_fp16_overflow 0
		.amdhsa_tg_split 0
		.amdhsa_exception_fp_ieee_invalid_op 0
		.amdhsa_exception_fp_denorm_src 0
		.amdhsa_exception_fp_ieee_div_zero 0
		.amdhsa_exception_fp_ieee_overflow 0
		.amdhsa_exception_fp_ieee_underflow 0
		.amdhsa_exception_fp_ieee_inexact 0
		.amdhsa_exception_int_div_zero 0
	.end_amdhsa_kernel

amdhsa.kernels:
  - .agpr_count:     0
    .args:
      - .offset:         0
        .size:           216
        .value_kind:     by_value
      - .offset:         216
        .size:           4
        .value_kind:     hidden_block_count_x
      - .offset:         220
        .size:           4
        .value_kind:     hidden_block_count_y
      - .offset:         224
        .size:           4
        .value_kind:     hidden_block_count_z
      - .offset:         228
        .size:           2
        .value_kind:     hidden_group_size_x
      - .offset:         230
        .size:           2
        .value_kind:     hidden_group_size_y
      - .offset:         232
        .size:           2
        .value_kind:     hidden_group_size_z
      - .offset:         234
        .size:           2
        .value_kind:     hidden_remainder_x
      - .offset:         236
        .size:           2
        .value_kind:     hidden_remainder_y
      - .offset:         238
        .size:           2
        .value_kind:     hidden_remainder_z
      - .offset:         256
        .size:           8
        .value_kind:     hidden_global_offset_x
      - .offset:         264
        .size:           8
        .value_kind:     hidden_global_offset_y
      - .offset:         272
        .size:           8
        .value_kind:     hidden_global_offset_z
      - .offset:         280
        .size:           2
        .value_kind:     hidden_grid_dims
      - .offset:         336
        .size:           4
        .value_kind:     hidden_dynamic_lds_size
    .group_segment_fixed_size: 0
    .kernarg_segment_align: 8
    .kernarg_segment_size: 472
    .language:       OpenCL C
    .language_version:
      - 2
      - 0
    .max_flat_workgroup_size: 512
    .name:           _Z3fwd4Args
    .private_segment_fixed_size: 0
    .sgpr_count:     108
    .sgpr_spill_count: 289
    .symbol:         _Z3fwd4Args.kd
    .uniform_work_group_size: 1
    .uses_dynamic_stack: false
    .vgpr_count:     256
    .vgpr_spill_count: 0
    .wavefront_size: 64
